# FFN-down epilogue: hoist the 8 serialized selgate loads (load+vmcnt0 ladder) into one batch at epilogue start
# speedup vs baseline: 1.0202x; 1.0202x over previous
.LBB0_1051:
	v_mov_b32_e32 v66, v0
	s_mov_b64 s[4:5], 0x40000
	v_ashrrev_i32_e32 v67, 2, v66
	v_and_b32_e32 v67, 0xffffffc0, v67
	v_lshl_add_u32 v67, s53, 8, v67
	v_and_or_b32 v138, v66, 15, v67
	v_lshrrev_b32_e32 v66, 1, v66
	v_ashrrev_i32_e32 v139, 31, v138
	v_and_b32_e32 v66, 0x78, v66
	v_lshl_add_u64 v[136:137], v[138:139], 2, s[10:11]
	v_lshl_or_b32 v140, s54, 8, v66
	global_load_dword v146, v[136:137], off
	global_load_dword v147, v[136:137], off offset:64
	global_load_dword v148, v[136:137], off offset:128
	global_load_dword v149, v[136:137], off offset:192
	global_load_dword v150, v[136:137], off offset:512
	global_load_dword v151, v[136:137], off offset:576
	global_load_dword v152, v[136:137], off offset:640
	global_load_dword v153, v[136:137], off offset:704
	v_ashrrev_i32_e32 v141, 31, v140
	v_lshlrev_b64 v[144:145], 11, v[138:139]
	s_waitcnt vmcnt(0)
	v_mul_f32_e32 v142, 0x3b800000, v146
	v_pk_mul_f32 v[68:69], v[128:129], v[142:143] op_sel_hi:[1,0]
	v_pk_mul_f32 v[66:67], v[126:127], v[142:143] op_sel_hi:[1,0]
	v_pk_mul_f32 v[124:125], v[124:125], v[142:143] op_sel_hi:[1,0]
	v_pk_mul_f32 v[122:123], v[122:123], v[142:143] op_sel_hi:[1,0]
	v_cvt_pk_bf16_f32 v66, v66, v67
	v_cvt_pk_bf16_f32 v67, v68, v69
	v_pk_mul_f32 v[116:117], v[116:117], v[142:143] op_sel_hi:[1,0]
	v_cvt_pk_bf16_f32 v68, v122, v123
	v_cvt_pk_bf16_f32 v69, v124, v125
	v_lshl_add_u64 v[122:123], s[12:13], 0, v[144:145]
	v_lshlrev_b64 v[124:125], 1, v[140:141]
	v_lshl_add_u64 v[122:123], v[122:123], 0, v[124:125]
	global_store_dwordx4 v[122:123], v[66:69], off
	v_pk_mul_f32 v[114:115], v[114:115], v[142:143] op_sel_hi:[1,0]
	s_nop 0
	v_pk_mul_f32 v[66:67], v[118:119], v[142:143] op_sel_hi:[1,0]
	v_pk_mul_f32 v[68:69], v[120:121], v[142:143] op_sel_hi:[1,0]
	v_cvt_pk_bf16_f32 v66, v66, v67
	s_nop 0
	v_cvt_pk_bf16_f32 v67, v68, v69
	v_cvt_pk_bf16_f32 v68, v114, v115
	v_cvt_pk_bf16_f32 v69, v116, v117
	global_store_dwordx4 v[122:123], v[66:69], off offset:256
	s_nop 1
	v_or_b32_e32 v66, 16, v138
	v_ashrrev_i32_e32 v67, 31, v66
	v_lshlrev_b64 v[116:117], 11, v[66:67]
	s_nop 1
	v_mul_f32_e32 v114, 0x3b800000, v147
	v_pk_mul_f32 v[68:69], v[112:113], v[114:115] op_sel_hi:[1,0]
	v_pk_mul_f32 v[66:67], v[110:111], v[114:115] op_sel_hi:[1,0]
	v_pk_mul_f32 v[106:107], v[106:107], v[114:115] op_sel_hi:[1,0]
	v_cvt_pk_bf16_f32 v66, v66, v67
	v_cvt_pk_bf16_f32 v67, v68, v69
	v_pk_mul_f32 v[108:109], v[108:109], v[114:115] op_sel_hi:[1,0]
	v_cvt_pk_bf16_f32 v68, v106, v107
	v_lshl_add_u64 v[106:107], s[12:13], 0, v[116:117]
	v_lshl_add_u64 v[106:107], v[106:107], 0, v[124:125]
	v_cvt_pk_bf16_f32 v69, v108, v109
	global_store_dwordx4 v[106:107], v[66:69], off
	v_pk_mul_f32 v[100:101], v[100:101], v[114:115] op_sel_hi:[1,0]
	v_pk_mul_f32 v[98:99], v[98:99], v[114:115] op_sel_hi:[1,0]
	v_pk_mul_f32 v[66:67], v[102:103], v[114:115] op_sel_hi:[1,0]
	v_pk_mul_f32 v[68:69], v[104:105], v[114:115] op_sel_hi:[1,0]
	v_cvt_pk_bf16_f32 v66, v66, v67
	s_nop 0
	v_cvt_pk_bf16_f32 v67, v68, v69
	v_cvt_pk_bf16_f32 v68, v98, v99
	v_cvt_pk_bf16_f32 v69, v100, v101
	global_store_dwordx4 v[106:107], v[66:69], off offset:256
	s_nop 1
	v_or_b32_e32 v66, 32, v138
	v_ashrrev_i32_e32 v67, 31, v66
	v_lshlrev_b64 v[100:101], 11, v[66:67]
	s_nop 1
	v_mul_f32_e32 v98, 0x3b800000, v148
	v_pk_mul_f32 v[68:69], v[96:97], v[98:99] op_sel_hi:[1,0]
	v_pk_mul_f32 v[66:67], v[94:95], v[98:99] op_sel_hi:[1,0]
	v_pk_mul_f32 v[90:91], v[90:91], v[98:99] op_sel_hi:[1,0]
	v_cvt_pk_bf16_f32 v66, v66, v67
	v_cvt_pk_bf16_f32 v67, v68, v69
	v_pk_mul_f32 v[92:93], v[92:93], v[98:99] op_sel_hi:[1,0]
	v_cvt_pk_bf16_f32 v68, v90, v91
	v_lshl_add_u64 v[90:91], s[12:13], 0, v[100:101]
	v_lshl_add_u64 v[90:91], v[90:91], 0, v[124:125]
	v_cvt_pk_bf16_f32 v69, v92, v93
	global_store_dwordx4 v[90:91], v[66:69], off
	v_pk_mul_f32 v[84:85], v[84:85], v[98:99] op_sel_hi:[1,0]
	v_pk_mul_f32 v[82:83], v[82:83], v[98:99] op_sel_hi:[1,0]
	v_pk_mul_f32 v[66:67], v[86:87], v[98:99] op_sel_hi:[1,0]
	v_pk_mul_f32 v[68:69], v[88:89], v[98:99] op_sel_hi:[1,0]
	v_cvt_pk_bf16_f32 v66, v66, v67
	s_nop 0
	v_cvt_pk_bf16_f32 v67, v68, v69
	v_cvt_pk_bf16_f32 v68, v82, v83
	v_cvt_pk_bf16_f32 v69, v84, v85
	global_store_dwordx4 v[90:91], v[66:69], off offset:256
	s_nop 1
	v_or_b32_e32 v66, 48, v138
	v_ashrrev_i32_e32 v67, 31, v66
	v_lshlrev_b64 v[84:85], 11, v[66:67]
	s_nop 1
	v_mul_f32_e32 v82, 0x3b800000, v149
	v_pk_mul_f32 v[68:69], v[80:81], v[82:83] op_sel_hi:[1,0]
	v_pk_mul_f32 v[66:67], v[78:79], v[82:83] op_sel_hi:[1,0]
	v_pk_mul_f32 v[74:75], v[74:75], v[82:83] op_sel_hi:[1,0]
	v_cvt_pk_bf16_f32 v66, v66, v67
	v_cvt_pk_bf16_f32 v67, v68, v69
	v_pk_mul_f32 v[76:77], v[76:77], v[82:83] op_sel_hi:[1,0]
	v_cvt_pk_bf16_f32 v68, v74, v75
	v_lshl_add_u64 v[74:75], s[12:13], 0, v[84:85]
	v_cvt_pk_bf16_f32 v69, v76, v77
	v_lshl_add_u64 v[74:75], v[74:75], 0, v[124:125]
	global_store_dwordx4 v[74:75], v[66:69], off
	s_nop 1
	v_pk_mul_f32 v[68:69], v[70:71], v[82:83] op_sel_hi:[1,0]
	v_pk_mul_f32 v[70:71], v[12:13], v[82:83] op_sel_hi:[1,0]
	v_pk_mul_f32 v[12:13], v[10:11], v[82:83] op_sel_hi:[1,0]
	v_pk_mul_f32 v[66:67], v[72:73], v[82:83] op_sel_hi:[1,0]
	v_cvt_pk_bf16_f32 v10, v68, v69
	s_nop 0
	v_cvt_pk_bf16_f32 v11, v66, v67
	v_cvt_pk_bf16_f32 v12, v12, v13
	v_cvt_pk_bf16_f32 v13, v70, v71
	global_store_dwordx4 v[74:75], v[10:13], off offset:256
	s_nop 1
	v_mul_f32_e32 v66, 0x3b800000, v150
	v_pk_mul_f32 v[12:13], v[64:65], v[66:67] op_sel_hi:[1,0]
	v_pk_mul_f32 v[10:11], v[62:63], v[66:67] op_sel_hi:[1,0]
	v_pk_mul_f32 v[60:61], v[60:61], v[66:67] op_sel_hi:[1,0]
	v_pk_mul_f32 v[58:59], v[58:59], v[66:67] op_sel_hi:[1,0]
	v_cvt_pk_bf16_f32 v10, v10, v11
	v_cvt_pk_bf16_f32 v11, v12, v13
	v_pk_mul_f32 v[52:53], v[52:53], v[66:67] op_sel_hi:[1,0]
	v_cvt_pk_bf16_f32 v12, v58, v59
	v_cvt_pk_bf16_f32 v13, v60, v61
	v_add_co_u32_e32 v60, vcc, s88, v122
	v_lshl_add_u64 v[58:59], v[122:123], 0, s[4:5]
	s_nop 0
	v_addc_co_u32_e32 v61, vcc, 0, v123, vcc
	global_store_dwordx4 v[60:61], v[10:13], off
	v_pk_mul_f32 v[50:51], v[50:51], v[66:67] op_sel_hi:[1,0]
	s_mov_b64 s[4:5], 0x48000
	v_pk_mul_f32 v[12:13], v[56:57], v[66:67] op_sel_hi:[1,0]
	v_pk_mul_f32 v[10:11], v[54:55], v[66:67] op_sel_hi:[1,0]
	s_nop 0
	v_cvt_pk_bf16_f32 v10, v10, v11
	v_cvt_pk_bf16_f32 v11, v12, v13
	v_cvt_pk_bf16_f32 v12, v50, v51
	v_cvt_pk_bf16_f32 v13, v52, v53
	global_store_dwordx4 v[58:59], v[10:13], off offset:256
	s_nop 1
	v_mul_f32_e32 v50, 0x3b800000, v151
	v_pk_mul_f32 v[12:13], v[48:49], v[50:51] op_sel_hi:[1,0]
	v_pk_mul_f32 v[10:11], v[46:47], v[50:51] op_sel_hi:[1,0]
	v_pk_mul_f32 v[44:45], v[44:45], v[50:51] op_sel_hi:[1,0]
	v_pk_mul_f32 v[42:43], v[42:43], v[50:51] op_sel_hi:[1,0]
	v_cvt_pk_bf16_f32 v10, v10, v11
	v_cvt_pk_bf16_f32 v11, v12, v13
	v_pk_mul_f32 v[36:37], v[36:37], v[50:51] op_sel_hi:[1,0]
	v_cvt_pk_bf16_f32 v12, v42, v43
	v_cvt_pk_bf16_f32 v13, v44, v45
	v_add_co_u32_e32 v44, vcc, s94, v122
	v_lshl_add_u64 v[42:43], v[122:123], 0, s[4:5]
	s_nop 0
	v_addc_co_u32_e32 v45, vcc, 0, v123, vcc
	global_store_dwordx4 v[44:45], v[10:13], off
	v_pk_mul_f32 v[34:35], v[34:35], v[50:51] op_sel_hi:[1,0]
	s_mov_b64 s[4:5], 0x50000
	v_pk_mul_f32 v[12:13], v[40:41], v[50:51] op_sel_hi:[1,0]
	v_pk_mul_f32 v[10:11], v[38:39], v[50:51] op_sel_hi:[1,0]
	s_nop 0
	v_cvt_pk_bf16_f32 v10, v10, v11
	v_cvt_pk_bf16_f32 v11, v12, v13
	v_cvt_pk_bf16_f32 v12, v34, v35
	v_cvt_pk_bf16_f32 v13, v36, v37
	global_store_dwordx4 v[42:43], v[10:13], off offset:256
	s_nop 1
	v_mul_f32_e32 v34, 0x3b800000, v152
	v_pk_mul_f32 v[12:13], v[32:33], v[34:35] op_sel_hi:[1,0]
	v_pk_mul_f32 v[10:11], v[30:31], v[34:35] op_sel_hi:[1,0]
	v_pk_mul_f32 v[28:29], v[28:29], v[34:35] op_sel_hi:[1,0]
	v_pk_mul_f32 v[26:27], v[26:27], v[34:35] op_sel_hi:[1,0]
	v_cvt_pk_bf16_f32 v10, v10, v11
	v_cvt_pk_bf16_f32 v11, v12, v13
	v_pk_mul_f32 v[20:21], v[20:21], v[34:35] op_sel_hi:[1,0]
	v_cvt_pk_bf16_f32 v12, v26, v27
	v_cvt_pk_bf16_f32 v13, v28, v29
	v_add_co_u32_e32 v28, vcc, s89, v122
	v_lshl_add_u64 v[26:27], v[122:123], 0, s[4:5]
	s_nop 0
	v_addc_co_u32_e32 v29, vcc, 0, v123, vcc
	global_store_dwordx4 v[28:29], v[10:13], off
	v_pk_mul_f32 v[18:19], v[18:19], v[34:35] op_sel_hi:[1,0]
	s_mov_b64 s[4:5], 0x58000
	v_pk_mul_f32 v[12:13], v[24:25], v[34:35] op_sel_hi:[1,0]
	v_pk_mul_f32 v[10:11], v[22:23], v[34:35] op_sel_hi:[1,0]
	s_nop 0
	v_cvt_pk_bf16_f32 v10, v10, v11
	v_cvt_pk_bf16_f32 v11, v12, v13
	v_cvt_pk_bf16_f32 v12, v18, v19
	v_cvt_pk_bf16_f32 v13, v20, v21
	global_store_dwordx4 v[26:27], v[10:13], off offset:256
	s_nop 1
	v_mul_f32_e32 v18, 0x3b800000, v153
	v_pk_mul_f32 v[12:13], v[16:17], v[18:19] op_sel_hi:[1,0]
	v_pk_mul_f32 v[10:11], v[14:15], v[18:19] op_sel_hi:[1,0]
	v_pk_mul_f32 v[16:17], v[228:229], v[18:19] op_sel_hi:[1,0]
	v_cvt_pk_bf16_f32 v10, v10, v11
	v_cvt_pk_bf16_f32 v11, v12, v13
	v_pk_mul_f32 v[14:15], v[230:231], v[18:19] op_sel_hi:[1,0]
	v_cvt_pk_bf16_f32 v12, v16, v17
	v_add_co_u32_e32 v16, vcc, s95, v122
	v_cvt_pk_bf16_f32 v13, v14, v15
	v_lshl_add_u64 v[14:15], v[122:123], 0, s[4:5]
	s_nop 0
	v_addc_co_u32_e32 v17, vcc, 0, v123, vcc
	global_store_dwordx4 v[16:17], v[10:13], off
	s_mov_b64 s[4:5], -1
	s_and_b64 vcc, exec, s[2:3]
	v_pk_mul_f32 v[10:11], v[4:5], v[18:19] op_sel_hi:[1,0]
	v_pk_mul_f32 v[4:5], v[2:3], v[18:19] op_sel_hi:[1,0]
	v_pk_mul_f32 v[8:9], v[8:9], v[18:19] op_sel_hi:[1,0]
	v_pk_mul_f32 v[6:7], v[6:7], v[18:19] op_sel_hi:[1,0]
	s_nop 0
	v_cvt_pk_bf16_f32 v2, v6, v7
	v_cvt_pk_bf16_f32 v3, v8, v9
	v_cvt_pk_bf16_f32 v4, v4, v5
	v_cvt_pk_bf16_f32 v5, v10, v11
	global_store_dwordx4 v[14:15], v[2:5], off offset:256
	s_cbranch_vccnz .LBB0_1035
	s_andn2_b64 vcc, exec, s[8:9]
	s_cbranch_vccnz .LBB0_1034
	s_barrier
	s_branch .LBB0_1034
